# attention KV loop: removed 15 redundant zero-initialisations of the fp8 pack registers (both 16-bit halves are always written by the two cvt_pk_fp8)
# baseline (speedup 1.0000x reference)
; __device__ __forceinline__ void partialSM_shift(f32x16& p0, f32x16& p1, float& m_reg, float& alpha) {
;     float pmax;
;     { float ma = fmaxf(p0[0], p0[1]), mb = fmaxf(p0[8], p0[9]), mc = fmaxf(p1[0], p1[1]), md = fmaxf(p1[8], p1[9]);
; #pragma unroll
;       for (int r = 2; r < 8; r += 2) { ma = fmaxf(fmaxf(ma, p0[r]), p0[r + 1]); mb = fmaxf(fmaxf(mb, p0[8 + r]), p0[9 + r]); mc = fmaxf(fmaxf(mc, p1[r]), p1[r + 1]); md = fmaxf(fmaxf(md, p1[8 + r]), p1[9 + r]); }
;       pmax = fmaxf(fmaxf(ma, mb), fmaxf(mc, md)); }
;     { auto rr = __builtin_amdgcn_permlane32_swap(__float_as_uint(pmax), __float_as_uint(pmax), false, false);
;       pmax = fmaxf(__uint_as_float(rr[0]), __uint_as_float(rr[1])); }
;     if (__builtin_expect(__all(pmax <= THR), 1)) { alpha = 1.f; }
;     else { const float d = fmaxf(pmax, 0.f); alpha = __builtin_amdgcn_exp2f(-d); m_reg += d;
; #pragma unroll
;         for (int r = 0; r < 16; ++r) p0[r] = p0[r] - d;
; #pragma unroll
;         for (int r = 0; r < 16; ++r) p1[r] = p1[r] - d; }
; #pragma unroll
;     for (int r = 0; r < 16; ++r) p0[r] = __builtin_amdgcn_exp2f(p0[r]);
; }
; __device__ __forceinline__ void finishSM(f32x16& p0, f32x16& p1, float alpha, float& l_reg, pg8::i32x8& pa) {
; #pragma unroll
;     for (int r = 0; r < 16; ++r) p1[r] = __builtin_amdgcn_exp2f(p1[r]);
;     float ps;
;     { float sa = p0[0] + p0[1], sb = p0[8] + p0[9], sc = p1[0] + p1[1], sd = p1[8] + p1[9];
; #pragma unroll
;       for (int r = 2; r < 8; ++r) { sa += p0[r]; sb += p0[8 + r]; sc += p1[r]; sd += p1[8 + r]; }
;       ps = (sa + sb) + (sc + sd); }
;     { auto rr = __builtin_amdgcn_permlane32_swap(__float_as_uint(ps), __float_as_uint(ps), false, false);
;       ps = __uint_as_float(rr[0]) + __uint_as_float(rr[1]); }
;     l_reg = l_reg * alpha + ps;
;     ...
;     pa = (pg8::i32x8){PK8(p0, 0), PK8(p0, 4), PK8(p0, 8), PK8(p0, 12), PK8(p1, 0), PK8(p1, 4), PK8(p1, 8), PK8(p1, 12)};
;     ...
; }
; __device__ __forceinline__ void qkt(f32x16& p0, f32x16& p1, const int kb, const pg8::i32x8 (&qf)[3], float minit) {
; #pragma unroll
;     for (int r = 0; r < 16; ++r) { p0[r] = -minit; p1[r] = -minit; }
; #pragma unroll
;     for (int s = 0; s < 3; ++s) {
;         const u32x4 a0 = *reinterpret_cast<const LAS u32x4*>((uintptr_t)(unsigned)(kb + (s * 64))), a1 = *reinterpret_cast<const LAS u32x4*>((uintptr_t)(unsigned)(kb + (s * 64 + 16)));
.LBB0_2158:
	s_waitcnt vmcnt(0)
	v_lshl_add_u64 v[82:83], v[174:175], 0, s[16:17]
	global_load_dwordx4 v[158:161], v[82:83], off
	global_load_dwordx4 v[154:157], v[176:177], off
	global_load_dwordx4 v[150:153], v[178:179], off
	s_mov_b32 s49, s47
	s_mov_b32 s47, s6
	s_mul_i32 s6, s48, 0x2800
	s_mul_i32 s50, s48, 0x3400
	v_add_u32_e32 v82, s6, v184
	s_add_i32 s6, s50, 0
	s_waitcnt vmcnt(4)
	ds_write_b128 v82, v[146:149]
	v_add_u32_e32 v82, s6, v168
	ds_write_b128 v82, v[138:141] offset:30720
	v_add_u32_e32 v82, s6, v170
	s_waitcnt vmcnt(3)
	ds_write_b128 v82, v[142:145] offset:30720
	s_mul_i32 s6, s49, 0x3400
	v_add_u32_e32 v146, s6, v183
	ds_read_b128 v[138:141], v146
	ds_read_b128 v[142:145], v146 offset:16
	v_xor_b32_e32 v82, 0x80000000, v185
	v_mov_b32_e32 v83, v82
	v_mov_b32_e32 v84, v82
	v_mov_b32_e32 v85, v82
	v_mov_b32_e32 v86, v82
	v_mov_b32_e32 v87, v82
	v_mov_b32_e32 v88, v82
	v_mov_b32_e32 v89, v82
	v_mov_b32_e32 v90, v82
	v_mov_b32_e32 v91, v82
	v_mov_b32_e32 v92, v82
	v_mov_b32_e32 v93, v82
	v_mov_b32_e32 v94, v82
	v_mov_b32_e32 v95, v82
	v_mov_b32_e32 v96, v82
	v_mov_b32_e32 v97, v82
	v_exp_f32_e32 v66, v66
	v_exp_f32_e32 v67, v67
	s_waitcnt lgkmcnt(0)
	v_mfma_f32_32x32x64_f8f6f4 v[98:113], v[138:145], v[130:137], v[82:97]
	ds_read_b128 v[138:141], v146 offset:6656
	ds_read_b128 v[142:145], v146 offset:6672
	ds_read_b128 v[206:209], v146 offset:64
	ds_read_b128 v[210:213], v146 offset:80
	ds_read_b128 v[214:217], v146 offset:6720
	ds_read_b128 v[218:221], v146 offset:6736
	ds_read_b128 v[222:225], v146 offset:128
	ds_read_b128 v[226:229], v146 offset:144
	v_exp_f32_e32 v230, v74
	v_exp_f32_e32 v75, v75
	v_exp_f32_e32 v76, v76
	v_exp_f32_e32 v147, v69
	v_exp_f32_e32 v77, v77
	v_exp_f32_e32 v148, v70
	v_exp_f32_e32 v78, v78
	v_exp_f32_e32 v149, v71
	v_exp_f32_e32 v79, v79
	v_add_f32_e32 v69, v200, v204
	v_add_f32_e32 v70, v66, v67
	v_add_f32_e32 v71, v230, v75
	v_exp_f32_e32 v188, v72
	v_exp_f32_e32 v80, v80
	s_waitcnt lgkmcnt(6)
	v_mfma_f32_32x32x64_f8f6f4 v[82:97], v[138:145], v[130:137], v[82:97]
	ds_read_b128 v[138:141], v146 offset:6784
	ds_read_b128 v[142:145], v146 offset:6800
	v_exp_f32_e32 v146, v68
	v_add_f32_e32 v68, v198, v202
	v_add_f32_e32 v68, v190, v68
	v_add_f32_e32 v69, v194, v69
	v_add_f32_e32 v70, v146, v70
	v_add_f32_e32 v71, v76, v71
	v_exp_f32_e32 v189, v73
	v_exp_f32_e32 v81, v81
	v_add_f32_e32 v68, v191, v68
	v_add_f32_e32 v69, v195, v69
	v_add_f32_e32 v70, v147, v70
	v_add_f32_e32 v71, v77, v71
	v_add_f32_e32 v68, v199, v68
	v_add_f32_e32 v69, v201, v69
	s_waitcnt lgkmcnt(6)
	v_mfma_f32_32x32x64_f8f6f4 v[98:113], v[206:213], v[122:129], v[98:113]
	v_add_f32_e32 v70, v148, v70
	v_add_f32_e32 v71, v78, v71
	v_add_f32_e32 v68, v203, v68
	v_add_f32_e32 v69, v205, v69
	v_add_f32_e32 v70, v149, v70
	v_add_f32_e32 v71, v79, v71
	v_add_f32_e32 v68, v192, v68
	v_add_f32_e32 v69, v196, v69
	v_add_f32_e32 v70, v188, v70
	v_add_f32_e32 v71, v80, v71
	v_add_f32_e32 v68, v193, v68
	v_add_f32_e32 v69, v197, v69
	v_add_f32_e32 v70, v189, v70
	v_add_f32_e32 v71, v81, v71
	s_waitcnt lgkmcnt(4)
	v_mfma_f32_32x32x64_f8f6f4 v[82:97], v[214:221], v[122:129], v[82:97]
	v_add_f32_e32 v68, v69, v68
	v_add_f32_e32 v69, v71, v70
	v_cvt_pk_fp8_f32 v73, v148, v149
	v_add_f32_e32 v187, v68, v69
	v_cvt_pk_fp8_f32 v74, v230, v75
	v_cvt_pk_fp8_f32 v68, v198, v202
	v_cvt_pk_fp8_f32 v69, v199, v203
	v_cvt_pk_fp8_f32 v70, v200, v204
	s_waitcnt lgkmcnt(2)
	v_mfma_f32_32x32x64_f8f6f4 v[98:113], v[222:229], v[114:121], v[98:113]
	v_cvt_pk_fp8_f32 v71, v201, v205
	v_cvt_pk_fp8_f32 v72, v66, v67
	v_cvt_pk_fp8_f32 v75, v78, v79
	v_cvt_pk_fp8_f32 v73, v188, v189 op_sel:[0,0,1]
	v_mov_b32_e32 v188, v187
	s_nop 1
	v_permlane32_swap_b32_e32 v187, v188
	v_cvt_pk_fp8_f32 v68, v190, v191 op_sel:[0,0,1]
	v_cvt_pk_fp8_f32 v69, v192, v193 op_sel:[0,0,1]
	v_cvt_pk_fp8_f32 v70, v194, v195 op_sel:[0,0,1]
	v_cvt_pk_fp8_f32 v71, v196, v197 op_sel:[0,0,1]
	v_cvt_pk_fp8_f32 v72, v146, v147 op_sel:[0,0,1]
	v_cvt_pk_fp8_f32 v74, v76, v77 op_sel:[0,0,1]
	v_cvt_pk_fp8_f32 v75, v80, v81 op_sel:[0,0,1]
	s_waitcnt lgkmcnt(0)
	v_mfma_f32_32x32x64_f8f6f4 v[82:97], v[138:145], v[114:121], v[82:97]
	s_mul_i32 s51, s47, 0x2800
	v_add_u32_e32 v66, s51, v171
	ds_read_b128 v[138:141], v66
	ds_read_b128 v[142:145], v66 offset:16
	v_max_f32_e32 v67, v98, v98
	v_max_f32_e32 v76, v106, v106
	s_nop 13
	v_max_f32_e32 v77, v90, v90
	v_mov_b32_e32 v189, 1.0
	s_waitcnt lgkmcnt(0)
	v_mfma_f32_32x32x64_f8f6f4 v[2:17], v[68:75], v[138:145], v[2:17]
	ds_read_b128 v[138:141], v66 offset:2560
	ds_read_b128 v[142:145], v66 offset:2576
	ds_read_b128 v[190:193], v66 offset:5120
	ds_read_b128 v[194:197], v66 offset:5136
	ds_read_b128 v[198:201], v66 offset:7680
	ds_read_b128 v[202:205], v66 offset:7696
	v_max_f32_e32 v66, v99, v99
	v_max_f32_e32 v66, v67, v66
	v_max_f32_e32 v67, v107, v107
	v_max_f32_e32 v67, v76, v67
	v_max_f32_e32 v76, v91, v91
	v_max_f32_e32 v76, v77, v76
	v_max3_f32 v77, v82, v83, v84
	v_max3_f32 v76, v76, v92, v93
	v_max3_f32 v66, v66, v100, v101
	v_max3_f32 v67, v67, v108, v109
	v_max3_f32 v77, v77, v85, v86
	v_max3_f32 v76, v76, v94, v95
	v_max3_f32 v66, v66, v102, v103
	v_max3_f32 v67, v67, v110, v111
	s_waitcnt lgkmcnt(4)
	v_mfma_f32_32x32x64_f8f6f4 v[50:65], v[68:75], v[138:145], v[50:65]
	v_max3_f32 v77, v77, v87, v88
	v_max3_f32 v76, v76, v96, v97
	v_max3_f32 v66, v66, v104, v105
	v_max3_f32 v67, v67, v112, v113
	v_max3_f32 v76, v77, v89, v76
	v_max3_f32 v66, v66, v67, v76
	v_mov_b32_e32 v67, v66
	s_nop 1
	v_permlane32_swap_b32_e32 v66, v67
	v_max_f32_e32 v67, v67, v67
	v_max_f32_e32 v66, v66, v66
	v_max_f32_e32 v66, v66, v67
	v_cmp_ge_f32_e32 vcc, s43, v66
	s_cmp_eq_u64 vcc, exec
	s_waitcnt lgkmcnt(2)
	v_mfma_f32_32x32x64_f8f6f4 v[34:49], v[68:75], v[190:197], v[34:49]
	s_waitcnt lgkmcnt(0)
	v_mfma_f32_32x32x64_f8f6f4 v[18:33], v[68:75], v[198:205], v[18:33]
	s_cbranch_scc0 .LBB0_2170
	v_cmp_gt_f32_e32 vcc, 1.0, v189
	s_cbranch_vccz .LBB0_2163

; __device__ __forceinline__ void partialSM_shift(f32x16& p0, f32x16& p1, float& m_reg, float& alpha) {
;     float pmax;
;     { float ma = fmaxf(p0[0], p0[1]), mb = fmaxf(p0[8], p0[9]), mc = fmaxf(p1[0], p1[1]), md = fmaxf(p1[8], p1[9]);
; #pragma unroll
;       for (int r = 2; r < 8; r += 2) { ma = fmaxf(fmaxf(ma, p0[r]), p0[r + 1]); mb = fmaxf(fmaxf(mb, p0[8 + r]), p0[9 + r]); mc = fmaxf(fmaxf(mc, p1[r]), p1[r + 1]); md = fmaxf(fmaxf(md, p1[8 + r]), p1[9 + r]); }
;       pmax = fmaxf(fmaxf(ma, mb), fmaxf(mc, md)); }
;     { auto rr = __builtin_amdgcn_permlane32_swap(__float_as_uint(pmax), __float_as_uint(pmax), false, false);
;       pmax = fmaxf(__uint_as_float(rr[0]), __uint_as_float(rr[1])); }
;     if (__builtin_expect(__all(pmax <= THR), 1)) { alpha = 1.f; }
;     else { const float d = fmaxf(pmax, 0.f); alpha = __builtin_amdgcn_exp2f(-d); m_reg += d;
; #pragma unroll
;         for (int r = 0; r < 16; ++r) p0[r] = p0[r] - d;
; #pragma unroll
;         for (int r = 0; r < 16; ++r) p1[r] = p1[r] - d; }
; #pragma unroll
;     for (int r = 0; r < 16; ++r) p0[r] = __builtin_amdgcn_exp2f(p0[r]);
; }
; __device__ __forceinline__ void finishSM(f32x16& p0, f32x16& p1, float alpha, float& l_reg, pg8::i32x8& pa) {
; #pragma unroll
;     for (int r = 0; r < 16; ++r) p1[r] = __builtin_amdgcn_exp2f(p1[r]);
;     float ps;
;     { float sa = p0[0] + p0[1], sb = p0[8] + p0[9], sc = p1[0] + p1[1], sd = p1[8] + p1[9];
; #pragma unroll
;       for (int r = 2; r < 8; ++r) { sa += p0[r]; sb += p0[8 + r]; sc += p1[r]; sd += p1[8 + r]; }
;       ps = (sa + sb) + (sc + sd); }
;     { auto rr = __builtin_amdgcn_permlane32_swap(__float_as_uint(ps), __float_as_uint(ps), false, false);
;       ps = __uint_as_float(rr[0]) + __uint_as_float(rr[1]); }
;     l_reg = l_reg * alpha + ps;
;     ...
;     pa = (pg8::i32x8){PK8(p0, 0), PK8(p0, 4), PK8(p0, 8), PK8(p0, 12), PK8(p1, 0), PK8(p1, 4), PK8(p1, 8), PK8(p1, 12)};
;     ...
; }
; __device__ __forceinline__ void qkt(f32x16& p0, f32x16& p1, const int kb, const pg8::i32x8 (&qf)[3], float minit) {
; #pragma unroll
;     for (int r = 0; r < 16; ++r) { p0[r] = -minit; p1[r] = -minit; }
; #pragma unroll
;     for (int s = 0; s < 3; ++s) {
;         const u32x4 a0 = *reinterpret_cast<const LAS u32x4*>((uintptr_t)(unsigned)(kb + (s * 64))), a1 = *reinterpret_cast<const LAS u32x4*>((uintptr_t)(unsigned)(kb + (s * 64 + 16)));
.LBB0_2163:
	s_mul_i32 s6, s47, 0x3400
	s_add_i32 s52, s6, 0
	s_add_i32 s6, s16, 0xc693ff80
	s_min_u32 s6, s6, 0x1000
	s_mul_i32 s18, s6, 0x600
	s_add_i32 s18, s18, 0x48000
	s_add_u32 s18, s14, s18
	s_barrier
	s_waitcnt vmcnt(0)
	v_lshl_add_u64 v[66:67], v[172:173], 0, s[6:7]
	s_addc_u32 s19, s15, 0
	v_lshl_add_u64 v[68:69], s[18:19], 0, v[162:163]
	global_load_dwordx4 v[146:149], v[66:67], off offset:192
	global_load_dwordx4 v[138:141], v[68:69], off
	v_lshl_add_u64 v[66:67], s[18:19], 0, v[166:167]
	global_load_dwordx4 v[142:145], v[66:67], off
	v_add_u32_e32 v66, s51, v184
	s_waitcnt vmcnt(5)
	ds_write_b128 v66, v[158:161]
	v_add_u32_e32 v66, s52, v168
	s_waitcnt vmcnt(4)
	ds_write_b128 v66, v[154:157] offset:30720
	v_add_u32_e32 v66, s52, v170
	v_exp_f32_e32 v222, v98
	v_exp_f32_e32 v223, v99
	v_exp_f32_e32 v224, v100
	v_exp_f32_e32 v225, v101
	v_exp_f32_e32 v226, v102
	v_exp_f32_e32 v227, v103
	v_exp_f32_e32 v228, v104
	v_exp_f32_e32 v229, v105
	v_exp_f32_e32 v230, v106
	v_exp_f32_e32 v231, v107
	v_exp_f32_e32 v232, v108
	v_exp_f32_e32 v233, v109
	v_exp_f32_e32 v234, v110
	v_exp_f32_e32 v235, v111
	v_exp_f32_e32 v236, v112
	v_exp_f32_e32 v237, v113
	s_waitcnt vmcnt(3)
	ds_write_b128 v66, v[150:153] offset:30720
	v_add_u32_e32 v158, s50, v183
	ds_read_b128 v[150:153], v158
	ds_read_b128 v[154:157], v158 offset:16
	v_xor_b32_e32 v66, 0x80000000, v185
	v_mov_b32_e32 v67, v66
	v_mov_b32_e32 v68, v66
	v_mov_b32_e32 v69, v66
	v_mov_b32_e32 v70, v66
	v_mov_b32_e32 v71, v66
	v_mov_b32_e32 v72, v66
	v_mov_b32_e32 v73, v66
	v_mov_b32_e32 v74, v66
	v_mov_b32_e32 v75, v66
	v_mov_b32_e32 v76, v66
	v_mov_b32_e32 v77, v66
	v_mov_b32_e32 v78, v66
	v_mov_b32_e32 v79, v66
	v_mov_b32_e32 v80, v66
	v_mov_b32_e32 v81, v66
	v_exp_f32_e32 v83, v83
	v_exp_f32_e32 v84, v84
	s_waitcnt lgkmcnt(0)
	v_mfma_f32_32x32x64_f8f6f4 v[98:113], v[150:157], v[130:137], v[66:81]
	ds_read_b128 v[150:153], v158 offset:6656
	ds_read_b128 v[154:157], v158 offset:6672
	ds_read_b128 v[190:193], v158 offset:64
	ds_read_b128 v[194:197], v158 offset:80
	ds_read_b128 v[198:201], v158 offset:6720
	ds_read_b128 v[202:205], v158 offset:6736
	ds_read_b128 v[206:209], v158 offset:128
	ds_read_b128 v[210:213], v158 offset:144
	ds_read_b128 v[214:217], v158 offset:6784
	ds_read_b128 v[218:221], v158 offset:6800
	v_exp_f32_e32 v85, v85
	v_exp_f32_e32 v158, v93
	v_exp_f32_e32 v94, v94
	v_exp_f32_e32 v95, v95
	v_exp_f32_e32 v96, v96
	v_exp_f32_e32 v97, v97
	v_mov_b32_e32 v93, 0
	v_cvt_pk_fp8_f32 v93, v94, v95
	v_cvt_pk_fp8_f32 v93, v96, v97 op_sel:[0,0,1]
	s_waitcnt lgkmcnt(8)
	v_mfma_f32_32x32x64_f8f6f4 v[66:81], v[150:157], v[130:137], v[66:81]
	v_exp_f32_e32 v150, v82
	v_exp_f32_e32 v155, v90
	v_exp_f32_e32 v156, v91
	v_exp_f32_e32 v157, v92
	v_exp_f32_e32 v151, v86
	v_exp_f32_e32 v152, v87
	v_exp_f32_e32 v153, v88
	v_add_f32_e32 v82, v223, v222
	v_add_f32_e32 v86, v231, v230
	v_add_f32_e32 v87, v150, v83
	v_add_f32_e32 v88, v155, v156
	v_add_f32_e32 v82, v224, v82
	v_add_f32_e32 v86, v232, v86
	v_add_f32_e32 v87, v84, v87
	v_add_f32_e32 v88, v157, v88
	s_waitcnt lgkmcnt(6)
	v_mfma_f32_32x32x64_f8f6f4 v[98:113], v[190:197], v[122:129], v[98:113]
	v_exp_f32_e32 v154, v89
	v_add_f32_e32 v82, v225, v82
	v_add_f32_e32 v86, v233, v86
	v_add_f32_e32 v87, v85, v87
	v_add_f32_e32 v88, v158, v88
	v_add_f32_e32 v82, v226, v82
	v_add_f32_e32 v86, v234, v86
	v_add_f32_e32 v87, v151, v87
	v_add_f32_e32 v88, v94, v88
	v_add_f32_e32 v82, v227, v82
	v_add_f32_e32 v86, v235, v86
	v_add_f32_e32 v87, v152, v87
	v_add_f32_e32 v88, v95, v88
	v_add_f32_e32 v82, v228, v82
	v_add_f32_e32 v86, v236, v86
	s_waitcnt lgkmcnt(4)
	v_mfma_f32_32x32x64_f8f6f4 v[66:81], v[198:205], v[122:129], v[66:81]
	v_add_f32_e32 v87, v153, v87
	v_add_f32_e32 v88, v96, v88
	v_add_f32_e32 v82, v229, v82
	v_add_f32_e32 v86, v237, v86
	v_add_f32_e32 v87, v154, v87
	v_add_f32_e32 v88, v97, v88
	v_add_f32_e32 v82, v86, v82
	v_add_f32_e32 v86, v88, v87
	v_add_f32_e32 v82, v82, v86
	s_waitcnt lgkmcnt(2)
	v_mfma_f32_32x32x64_f8f6f4 v[98:113], v[206:213], v[114:121], v[98:113]
	v_cvt_pk_fp8_f32 v86, v222, v223
	v_cvt_pk_fp8_f32 v87, v226, v227
	v_cvt_pk_fp8_f32 v88, v230, v231
	v_cvt_pk_fp8_f32 v89, v234, v235
	v_cvt_pk_fp8_f32 v90, v150, v83
	v_cvt_pk_fp8_f32 v91, v151, v152
	v_cvt_pk_fp8_f32 v92, v155, v156
	v_mov_b32_e32 v83, v82
	s_nop 1
	v_permlane32_swap_b32_e32 v82, v83
	v_cvt_pk_fp8_f32 v86, v224, v225 op_sel:[0,0,1]
	v_cvt_pk_fp8_f32 v87, v228, v229 op_sel:[0,0,1]
	v_cvt_pk_fp8_f32 v88, v232, v233 op_sel:[0,0,1]
	v_cvt_pk_fp8_f32 v89, v236, v237 op_sel:[0,0,1]
	s_waitcnt lgkmcnt(0)
	v_mfma_f32_32x32x64_f8f6f4 v[66:81], v[214:221], v[114:121], v[66:81]
	v_cvt_pk_fp8_f32 v90, v84, v85 op_sel:[0,0,1]
	v_cvt_pk_fp8_f32 v91, v153, v154 op_sel:[0,0,1]
	v_cvt_pk_fp8_f32 v92, v157, v158 op_sel:[0,0,1]
	s_mul_i32 s6, s49, 0x2800
	v_add_u32_e32 v84, s6, v171
	ds_read_b128 v[150:153], v84
	ds_read_b128 v[154:157], v84 offset:16
	v_max_f32_e32 v85, v98, v98
	v_max_f32_e32 v94, v106, v106
	s_nop 10
	v_max_f32_e32 v95, v74, v74
	s_waitcnt lgkmcnt(0)
	v_mfma_f32_32x32x64_f8f6f4 v[2:17], v[86:93], v[150:157], v[2:17]
	ds_read_b128 v[150:153], v84 offset:2560
	ds_read_b128 v[154:157], v84 offset:2576
	ds_read_b128 v[190:193], v84 offset:5120
	ds_read_b128 v[194:197], v84 offset:5136
	ds_read_b128 v[198:201], v84 offset:7680
	ds_read_b128 v[202:205], v84 offset:7696
	v_max_f32_e32 v84, v99, v99
	v_max_f32_e32 v84, v85, v84
	v_max_f32_e32 v85, v107, v107
	v_max_f32_e32 v85, v94, v85
	v_max_f32_e32 v94, v75, v75
	v_max_f32_e32 v94, v95, v94
	v_max3_f32 v95, v66, v67, v68
	v_max3_f32 v94, v94, v76, v77
	v_max3_f32 v84, v84, v100, v101
	v_max3_f32 v85, v85, v108, v109
	v_max3_f32 v95, v95, v69, v70
	v_max3_f32 v94, v94, v78, v79
	v_max3_f32 v84, v84, v102, v103
	v_max3_f32 v85, v85, v110, v111
	s_waitcnt lgkmcnt(4)
	v_mfma_f32_32x32x64_f8f6f4 v[50:65], v[86:93], v[150:157], v[50:65]
	v_max3_f32 v95, v95, v71, v72
	v_max3_f32 v94, v94, v80, v81
	v_max3_f32 v84, v84, v104, v105
	v_max3_f32 v85, v85, v112, v113
	v_max3_f32 v94, v95, v73, v94
	v_max3_f32 v84, v84, v85, v94
	v_mov_b32_e32 v85, v84
	s_nop 1
	v_permlane32_swap_b32_e32 v84, v85
	v_max_f32_e32 v85, v85, v85
	v_max_f32_e32 v84, v84, v84
	v_max_f32_e32 v84, v84, v85
	v_cmp_ge_f32_e32 vcc, s43, v84
	s_cmp_eq_u64 vcc, exec
	v_mov_b32_e32 v150, 1.0
	s_waitcnt lgkmcnt(2)
	v_mfma_f32_32x32x64_f8f6f4 v[34:49], v[86:93], v[190:197], v[34:49]
	s_waitcnt lgkmcnt(0)
	v_mfma_f32_32x32x64_f8f6f4 v[18:33], v[86:93], v[198:205], v[18:33]
	s_cbranch_scc0 .LBB0_2171
	v_cmp_gt_f32_e32 vcc, 1.0, v150
	s_cbranch_vccz .LBB0_2168
